# P1 norm1/modulate: row and gain/scale/shift loads hoisted into free quads (36 in flight)
# speedup vs baseline: 1.0006x; 1.0006x over previous
.LBB0_387:
	s_nop 1
	global_load_dwordx4 v[108:111], v66, s[10:11]
	global_load_dwordx4 v[112:115], v66, s[10:11] offset:1024
	global_load_dwordx4 v[116:119], v66, s[10:11] offset:2048
	global_load_dwordx4 v[120:123], v66, s[10:11] offset:3072
	v_lshl_add_u64 v[2:3], s[10:11], 0, v[66:67]
	v_add_co_u32_e32 v84, vcc, 0x1000, v2
	s_waitcnt vmcnt(11)
	v_mov_b32_e32 v86, v63
	v_addc_co_u32_e32 v85, vcc, 0, v3, vcc
	global_load_dwordx4 v[14:17], v[84:85], off
	global_load_dwordx4 v[10:13], v[84:85], off offset:1024
	global_load_dwordx4 v[6:9], v[84:85], off offset:2048
	global_load_dwordx4 v[2:5], v[84:85], off offset:3072
	s_waitcnt vmcnt(14)
	v_mov_b32_e32 v87, v59
	v_mov_b32_e32 v84, v62
	v_mov_b32_e32 v85, v58
	v_pk_mul_f32 v[86:87], v[86:87], v[86:87]
	v_mov_b32_e32 v88, v65
	v_mov_b32_e32 v89, v61
	v_pk_fma_f32 v[84:85], v[84:85], v[84:85], v[86:87]
	v_mov_b32_e32 v86, v64
	v_mov_b32_e32 v87, v60
	v_pk_mul_f32 v[88:89], v[88:89], v[88:89]
	s_min_i32 s0, s24, 0x4000
	v_pk_fma_f32 v[86:87], v[86:87], v[86:87], v[88:89]
	s_waitcnt vmcnt(13)
	v_pk_mul_f32 v[88:89], v[54:55], v[54:55]
	v_pk_add_f32 v[84:85], v[84:85], v[86:87]
	v_pk_mul_f32 v[86:87], v[56:57], v[56:57]
	v_pk_add_f32 v[84:85], v[84:85], v[84:85] op_sel:[0,1] op_sel_hi:[1,0]
	v_pk_mov_b32 v[90:91], v[88:89], v[86:87] op_sel:[1,0]
	v_mov_b32_e32 v89, v87
	v_pk_add_f32 v[86:87], v[90:91], v[88:89]
	s_waitcnt vmcnt(11)
	v_mul_f32_e32 v88, v46, v46
	v_mul_f32_e32 v89, v47, v47
	v_pk_add_f32 v[86:87], v[86:87], v[86:87] op_sel:[0,1] op_sel_hi:[1,0]
	s_lshr_b32 s0, s0, 12
	v_mov_b32_e32 v85, v88
	v_mov_b32_e32 v87, v89
	s_mul_i32 s2, s0, 0x3000
	v_pk_add_f32 v[84:85], v[84:85], v[86:87]
	v_mul_f32_e32 v86, v51, v51
	v_mul_f32_e32 v88, v53, v53
	s_ashr_i32 s3, s2, 31
	v_mul_f32_e32 v90, v48, v48
	v_mul_f32_e32 v91, v49, v49
	v_pk_fma_f32 v[86:87], v[50:51], v[50:51], v[86:87] op_sel_hi:[1,1,0]
	v_pk_fma_f32 v[88:89], v[52:53], v[52:53], v[88:89] op_sel_hi:[1,1,0]
	s_lshl_b64 s[2:3], s[2:3], 2
	v_mov_b32_e32 v87, v90
	v_mov_b32_e32 v89, v91
	s_add_u32 s16, s9, s2
	v_pk_add_f32 v[86:87], v[86:87], v[88:89]
	s_addc_u32 s17, s20, s3
	global_load_dwordx4 v[132:135], v66, s[16:17]
	global_load_dwordx4 v[144:147], v66, s[16:17] offset:1024
	global_load_dwordx4 v[156:159], v66, s[16:17] offset:2048
	global_load_dwordx4 v[168:171], v66, s[16:17] offset:3072
	global_load_dwordx4 v[180:183], v80, s[16:17]
	global_load_dwordx4 v[192:195], v81, s[16:17]
	global_load_dwordx4 v[204:207], v82, s[16:17]
	global_load_dwordx4 v[216:219], v83, s[16:17]
	s_min_i32 s0, s14, 0x4000
	v_pk_add_f32 v[84:85], v[84:85], v[86:87]
	s_waitcnt vmcnt(10)
	v_pk_mul_f32 v[86:87], v[44:45], v[44:45]
	v_pk_mul_f32 v[88:89], v[42:43], v[42:43]
	s_lshr_b32 s0, s0, 12
	v_pk_mov_b32 v[90:91], v[88:89], v[86:87] op_sel:[1,0]
	v_mov_b32_e32 v89, v87
	s_mul_i32 s2, s0, 0x3000
	v_pk_add_f32 v[86:87], v[90:91], v[88:89]
	s_ashr_i32 s3, s2, 31
	s_waitcnt vmcnt(8)
	v_mul_f32_e32 v88, v26, v26
	v_mul_f32_e32 v89, v27, v27
	v_pk_add_f32 v[84:85], v[84:85], v[84:85] op_sel:[0,1] op_sel_hi:[1,0]
	v_pk_add_f32 v[86:87], v[86:87], v[86:87] op_sel:[0,1] op_sel_hi:[1,0]
	s_lshl_b64 s[2:3], s[2:3], 2
	v_mov_b32_e32 v85, v88
	v_mov_b32_e32 v87, v89
	s_add_u32 s10, s9, s2
	v_pk_add_f32 v[84:85], v[84:85], v[86:87]
	v_mul_f32_e32 v86, v39, v39
	v_mul_f32_e32 v88, v41, v41
	s_addc_u32 s11, s20, s3
	global_load_dwordx4 v[228:231], v66, s[10:11]
	global_load_dwordx4 v[240:243], v66, s[10:11] offset:1024
	v_mul_f32_e32 v90, v28, v28
	v_mul_f32_e32 v91, v29, v29
	v_pk_fma_f32 v[86:87], v[38:39], v[38:39], v[86:87] op_sel_hi:[1,1,0]
	v_pk_fma_f32 v[88:89], v[40:41], v[40:41], v[88:89] op_sel_hi:[1,1,0]
	s_add_u32 s18, s16, 0x2000
	v_mov_b32_e32 v87, v90
	v_mov_b32_e32 v89, v91
	s_addc_u32 s19, s17, 0
	global_load_dwordx4 v[124:127], v66, s[18:19]
	global_load_dwordx4 v[140:143], v77, s[18:19]
	global_load_dwordx4 v[152:155], v78, s[18:19]
	global_load_dwordx4 v[164:167], v79, s[18:19]
	global_load_dwordx4 v[176:179], v80, s[18:19]
	global_load_dwordx4 v[188:191], v81, s[18:19]
	global_load_dwordx4 v[200:203], v82, s[18:19]
	global_load_dwordx4 v[212:215], v83, s[18:19]
	v_pk_add_f32 v[86:87], v[86:87], v[88:89]
	s_waitcnt lgkmcnt(0)
	v_readfirstlane_b32 s12, v68
	v_readfirstlane_b32 s13, v69
	s_nop 5
	global_load_dwordx4 v[128:131], v66, s[12:13]
	global_load_dwordx4 v[136:139], v66, s[12:13] offset:1024
	global_load_dwordx4 v[148:151], v66, s[12:13] offset:2048
	global_load_dwordx4 v[160:163], v66, s[12:13] offset:3072
	global_load_dwordx4 v[172:175], v80, s[12:13]
	global_load_dwordx4 v[184:187], v81, s[12:13]
	global_load_dwordx4 v[196:199], v82, s[12:13]
	global_load_dwordx4 v[208:211], v83, s[12:13]
	global_load_dwordx4 v[220:223], v66, s[12:13]
	global_load_dwordx4 v[232:235], v66, s[12:13] offset:1024
	global_load_dwordx4 v[244:247], v66, s[12:13] offset:2048
	v_pk_add_f32 v[96:97], v[84:85], v[86:87]
	s_nop 2
	s_waitcnt vmcnt(36)
	v_mov_b32_e32 v34, v108
	v_mov_b32_e32 v35, v109
	v_mov_b32_e32 v36, v110
	v_mov_b32_e32 v37, v111
	global_load_dwordx4 v[108:111], v66, s[10:11] offset:2048
	v_mov_b32_e32 v100, v35
	s_waitcnt vmcnt(36)
	v_mov_b32_e32 v30, v112
	v_mov_b32_e32 v31, v113
	v_mov_b32_e32 v32, v114
	v_mov_b32_e32 v33, v115
	global_load_dwordx4 v[112:115], v66, s[12:13] offset:3072
	v_mov_b32_e32 v101, v31
	v_mov_b32_e32 v98, v34
	v_mov_b32_e32 v99, v30
	v_pk_mul_f32 v[100:101], v[100:101], v[100:101]
	v_mov_b32_e32 v102, v37
	v_mov_b32_e32 v103, v33
	v_pk_fma_f32 v[98:99], v[98:99], v[98:99], v[100:101]
	v_mov_b32_e32 v100, v36
	v_mov_b32_e32 v101, v32
	v_pk_mul_f32 v[102:103], v[102:103], v[102:103]
	s_waitcnt vmcnt(20)
	v_mov_b32_e32 v22, v116
	v_mov_b32_e32 v23, v117
	v_mov_b32_e32 v24, v118
	v_mov_b32_e32 v25, v119
	v_mov_b32_e32 v18, v120
	v_mov_b32_e32 v19, v121
	v_mov_b32_e32 v20, v122
	v_mov_b32_e32 v21, v123
	v_mov_b32_e32 v84, v124
	v_mov_b32_e32 v85, v125
	v_mov_b32_e32 v86, v126
	v_mov_b32_e32 v87, v127
	global_load_dwordx4 v[120:123], v66, s[10:11] offset:3072
	global_load_dwordx4 v[124:127], v80, s[12:13]
	v_pk_add_f32 v[86:87], v[86:87], 1.0 op_sel_hi:[1,0]
	v_pk_fma_f32 v[100:101], v[100:101], v[100:101], v[102:103]
	v_pk_mul_f32 v[102:103], v[22:23], v[22:23]
	v_pk_add_f32 v[98:99], v[98:99], v[100:101]
	v_pk_mul_f32 v[100:101], v[24:25], v[24:25]
	v_pk_add_f32 v[98:99], v[98:99], v[98:99] op_sel:[0,1] op_sel_hi:[1,0]
	v_pk_mov_b32 v[104:105], v[102:103], v[100:101] op_sel:[1,0]
	v_mov_b32_e32 v103, v101
	v_pk_add_f32 v[100:101], v[104:105], v[102:103]
	v_mul_f32_e32 v102, v14, v14
	v_mul_f32_e32 v103, v15, v15
	v_pk_add_f32 v[100:101], v[100:101], v[100:101] op_sel:[0,1] op_sel_hi:[1,0]
	v_mov_b32_e32 v99, v102
	v_mov_b32_e32 v101, v103
	v_pk_add_f32 v[98:99], v[98:99], v[100:101]
	v_mul_f32_e32 v100, v19, v19
	v_mul_f32_e32 v102, v21, v21
	v_mul_f32_e32 v104, v16, v16
	v_mul_f32_e32 v105, v17, v17
	v_pk_fma_f32 v[100:101], v[18:19], v[18:19], v[100:101] op_sel_hi:[1,1,0]
	v_pk_fma_f32 v[102:103], v[20:21], v[20:21], v[102:103] op_sel_hi:[1,1,0]
	v_mov_b32_e32 v101, v104
	v_mov_b32_e32 v103, v105
	v_pk_add_f32 v[100:101], v[100:101], v[102:103]
	v_pk_mul_f32 v[102:103], v[10:11], v[10:11]
	v_pk_add_f32 v[98:99], v[98:99], v[100:101]
	v_pk_mul_f32 v[100:101], v[12:13], v[12:13]
	v_pk_add_f32 v[98:99], v[98:99], v[98:99] op_sel:[0,1] op_sel_hi:[1,0]
	v_pk_mov_b32 v[104:105], v[102:103], v[100:101] op_sel:[1,0]
	v_mov_b32_e32 v103, v101
	v_pk_add_f32 v[100:101], v[104:105], v[102:103]
	v_mul_f32_e32 v102, v2, v2
	v_mul_f32_e32 v103, v3, v3
	v_pk_add_f32 v[100:101], v[100:101], v[100:101] op_sel:[0,1] op_sel_hi:[1,0]
	v_mov_b32_e32 v99, v102
	v_mov_b32_e32 v101, v103
	v_pk_add_f32 v[98:99], v[98:99], v[100:101]
	v_mul_f32_e32 v100, v7, v7
	v_mul_f32_e32 v102, v9, v9
	v_mul_f32_e32 v104, v4, v4
	v_mul_f32_e32 v105, v5, v5
	v_pk_fma_f32 v[100:101], v[6:7], v[6:7], v[100:101] op_sel_hi:[1,1,0]
	v_pk_fma_f32 v[102:103], v[8:9], v[8:9], v[102:103] op_sel_hi:[1,1,0]
	v_mov_b32_e32 v101, v104
	v_mov_b32_e32 v103, v105
	v_pk_add_f32 v[100:101], v[100:101], v[102:103]
	v_pk_add_f32 v[84:85], v[84:85], 1.0 op_sel_hi:[1,0]
	v_pk_add_f32 v[98:99], v[98:99], v[100:101]
	v_mov_b32_e32 v101, v96
	v_mov_b32_e32 v100, v98
	v_mov_b32_e32 v96, v99
	v_pk_add_f32 v[96:97], v[100:101], v[96:97]
	s_nop 1
	v_mov_b32_dpp v99, v97 quad_perm:[1,0,3,2] row_mask:0xf bank_mask:0xf bound_ctrl:1
	v_mov_b32_dpp v98, v96 quad_perm:[1,0,3,2] row_mask:0xf bank_mask:0xf bound_ctrl:1
	v_pk_add_f32 v[96:97], v[96:97], v[98:99]
	s_nop 1
	v_mov_b32_dpp v99, v97 quad_perm:[2,3,0,1] row_mask:0xf bank_mask:0xf bound_ctrl:1
	v_mov_b32_dpp v98, v96 quad_perm:[2,3,0,1] row_mask:0xf bank_mask:0xf bound_ctrl:1
	v_pk_add_f32 v[96:97], v[96:97], v[98:99]
	s_nop 1
	v_mov_b32_dpp v99, v97 row_half_mirror row_mask:0xf bank_mask:0xf bound_ctrl:1
	v_mov_b32_dpp v98, v96 row_half_mirror row_mask:0xf bank_mask:0xf bound_ctrl:1
	v_pk_add_f32 v[96:97], v[96:97], v[98:99]
	s_nop 1
	v_mov_b32_dpp v99, v97 row_mirror row_mask:0xf bank_mask:0xf bound_ctrl:1
	v_mov_b32_dpp v98, v96 row_mirror row_mask:0xf bank_mask:0xf bound_ctrl:1
	v_pk_add_f32 v[96:97], v[96:97], v[98:99]
	ds_bpermute_b32 v99, v1, v97
	ds_bpermute_b32 v98, v1, v96
	s_waitcnt lgkmcnt(0)
	v_pk_add_f32 v[96:97], v[96:97], v[98:99]
	ds_bpermute_b32 v99, v76, v97
	ds_bpermute_b32 v98, v76, v96
	s_waitcnt lgkmcnt(0)
	v_pk_add_f32 v[96:97], v[96:97], v[98:99]
	s_nop 0
	v_pk_fma_f32 v[96:97], v[96:97], s[8:9], v[74:75] op_sel_hi:[1,0,0]
	s_nop 0
	v_mul_f32_e32 v98, 0x4b800000, v97
	v_cmp_gt_f32_e32 vcc, s23, v97
	s_nop 1
	v_cndmask_b32_e32 v97, v97, v98, vcc
	v_rsq_f32_e32 v97, v97
	s_nop 0
	v_mul_f32_e32 v98, 0x45800000, v97
	v_cndmask_b32_e32 v98, v97, v98, vcc
	v_pk_mul_f32 v[64:65], v[64:65], v[98:99] op_sel_hi:[1,0]
	v_pk_mul_f32 v[62:63], v[62:63], v[98:99] op_sel_hi:[1,0]
	s_waitcnt vmcnt(14)
	v_mov_b32_e32 v88, v128
	v_mov_b32_e32 v89, v129
	v_mov_b32_e32 v90, v130
	v_mov_b32_e32 v91, v131
	v_pk_mul_f32 v[64:65], v[90:91], v[64:65]
	v_pk_mul_f32 v[62:63], v[88:89], v[62:63]
	s_waitcnt vmcnt(14)
	v_mov_b32_e32 v92, v132
	v_mov_b32_e32 v93, v133
	v_mov_b32_e32 v94, v134
	v_mov_b32_e32 v95, v135
	global_load_dwordx4 v[132:135], v80, s[10:11]
	v_pk_fma_f32 v[64:65], v[86:87], v[64:65], v[94:95]
	v_pk_fma_f32 v[62:63], v[84:85], v[62:63], v[92:93]
	v_pk_mul_f32 v[60:61], v[60:61], v[98:99] op_sel_hi:[1,0]
	v_cvt_pk_bf16_f32 v62, v62, v63
	v_cvt_pk_bf16_f32 v63, v64, v65
	global_store_dwordx2 v[72:73], v[62:63], off
	s_nop 0
	v_pk_mul_f32 v[58:59], v[58:59], v[98:99] op_sel_hi:[1,0]
	v_pk_mul_f32 v[56:57], v[56:57], v[98:99] op_sel_hi:[1,0]
	v_pk_mul_f32 v[54:55], v[54:55], v[98:99] op_sel_hi:[1,0]
	v_pk_mul_f32 v[52:53], v[52:53], v[98:99] op_sel_hi:[1,0]
	v_pk_mul_f32 v[50:51], v[50:51], v[98:99] op_sel_hi:[1,0]
	v_pk_mul_f32 v[48:49], v[48:49], v[98:99] op_sel_hi:[1,0]
	v_pk_mul_f32 v[46:47], v[46:47], v[98:99] op_sel_hi:[1,0]
	v_pk_mul_f32 v[44:45], v[44:45], v[98:99] op_sel_hi:[1,0]
	v_pk_mul_f32 v[42:43], v[42:43], v[98:99] op_sel_hi:[1,0]
	v_pk_mul_f32 v[40:41], v[40:41], v[98:99] op_sel_hi:[1,0]
	v_pk_mul_f32 v[38:39], v[38:39], v[98:99] op_sel_hi:[1,0]
	v_pk_mul_f32 v[28:29], v[28:29], v[98:99] op_sel_hi:[1,0]
	v_pk_mul_f32 v[26:27], v[26:27], v[98:99] op_sel_hi:[1,0]
	v_cmp_gt_f32_e32 vcc, s23, v96
	s_waitcnt vmcnt(15)
	v_mov_b32_e32 v62, v136
	v_mov_b32_e32 v63, v137
	v_mov_b32_e32 v64, v138
	v_mov_b32_e32 v65, v139
	s_nop 5
	global_load_dwordx4 v[136:139], v81, s[12:13]
	v_pk_mul_f32 v[58:59], v[62:63], v[58:59]
	v_pk_mul_f32 v[60:61], v[64:65], v[60:61]
	s_waitcnt vmcnt(16)
	v_mov_b32_e32 v84, v140
	v_mov_b32_e32 v85, v141
	v_mov_b32_e32 v86, v142
	v_mov_b32_e32 v87, v143
	v_pk_add_f32 v[62:63], v[86:87], 1.0 op_sel_hi:[1,0]
	v_pk_add_f32 v[64:65], v[84:85], 1.0 op_sel_hi:[1,0]
	s_waitcnt vmcnt(16)
	v_mov_b32_e32 v88, v144
	v_mov_b32_e32 v89, v145
	v_mov_b32_e32 v90, v146
	v_mov_b32_e32 v91, v147
	global_load_dwordx4 v[144:147], v81, s[10:11]
	v_pk_fma_f32 v[60:61], v[62:63], v[60:61], v[90:91]
	v_pk_fma_f32 v[58:59], v[64:65], v[58:59], v[88:89]
	s_nop 0
	v_cvt_pk_bf16_f32 v58, v58, v59
	v_cvt_pk_bf16_f32 v59, v60, v61
	global_store_dwordx2 v[72:73], v[58:59], off offset:512
	s_nop 0
	s_waitcnt vmcnt(17)
	v_mov_b32_e32 v58, v148
	v_mov_b32_e32 v59, v149
	v_mov_b32_e32 v60, v150
	v_mov_b32_e32 v61, v151
	global_load_dwordx4 v[148:151], v82, s[12:13]
	v_pk_mul_f32 v[54:55], v[58:59], v[54:55]
	v_pk_mul_f32 v[56:57], v[60:61], v[56:57]
	s_waitcnt vmcnt(18)
	v_mov_b32_e32 v62, v152
	v_mov_b32_e32 v63, v153
	v_mov_b32_e32 v64, v154
	v_mov_b32_e32 v65, v155
	v_pk_add_f32 v[58:59], v[64:65], 1.0 op_sel_hi:[1,0]
	v_pk_add_f32 v[60:61], v[62:63], 1.0 op_sel_hi:[1,0]
	s_waitcnt vmcnt(18)
	v_mov_b32_e32 v84, v156
	v_mov_b32_e32 v85, v157
	v_mov_b32_e32 v86, v158
	v_mov_b32_e32 v87, v159
	global_load_dwordx4 v[156:159], v82, s[10:11]
	v_pk_fma_f32 v[56:57], v[58:59], v[56:57], v[86:87]
	v_pk_fma_f32 v[54:55], v[60:61], v[54:55], v[84:85]
	s_nop 0
	v_cvt_pk_bf16_f32 v54, v54, v55
	v_cvt_pk_bf16_f32 v55, v56, v57
	global_store_dwordx2 v[72:73], v[54:55], off offset:1024
	s_nop 0
	s_waitcnt vmcnt(19)
	v_mov_b32_e32 v54, v160
	v_mov_b32_e32 v55, v161
	v_mov_b32_e32 v56, v162
	v_mov_b32_e32 v57, v163
	global_load_dwordx4 v[160:163], v83, s[12:13]
	v_pk_mul_f32 v[50:51], v[50:51], v[54:55]
	v_pk_mul_f32 v[52:53], v[52:53], v[56:57]
	s_waitcnt vmcnt(20)
	v_mov_b32_e32 v58, v164
	v_mov_b32_e32 v59, v165
	v_mov_b32_e32 v60, v166
	v_mov_b32_e32 v61, v167
	v_pk_add_f32 v[54:55], v[60:61], 1.0 op_sel_hi:[1,0]
	v_pk_add_f32 v[56:57], v[58:59], 1.0 op_sel_hi:[1,0]
	s_waitcnt vmcnt(20)
	v_mov_b32_e32 v62, v168
	v_mov_b32_e32 v63, v169
	v_mov_b32_e32 v64, v170
	v_mov_b32_e32 v65, v171
	global_load_dwordx4 v[168:171], v83, s[10:11]
	v_pk_fma_f32 v[52:53], v[52:53], v[54:55], v[64:65]
	v_pk_fma_f32 v[50:51], v[50:51], v[56:57], v[62:63]
	s_nop 0
	v_cvt_pk_bf16_f32 v50, v50, v51
	v_cvt_pk_bf16_f32 v51, v52, v53
	global_store_dwordx2 v[72:73], v[50:51], off offset:1536
	s_nop 0
	s_waitcnt vmcnt(21)
	v_mov_b32_e32 v50, v172
	v_mov_b32_e32 v51, v173
	v_mov_b32_e32 v52, v174
	v_mov_b32_e32 v53, v175
	v_pk_mul_f32 v[46:47], v[46:47], v[50:51]
	v_pk_mul_f32 v[48:49], v[48:49], v[52:53]
	s_waitcnt vmcnt(21)
	v_mov_b32_e32 v54, v176
	v_mov_b32_e32 v55, v177
	v_mov_b32_e32 v56, v178
	v_mov_b32_e32 v57, v179
	v_pk_add_f32 v[50:51], v[56:57], 1.0 op_sel_hi:[1,0]
	v_pk_add_f32 v[52:53], v[54:55], 1.0 op_sel_hi:[1,0]
	s_waitcnt vmcnt(21)
	v_mov_b32_e32 v58, v180
	v_mov_b32_e32 v59, v181
	v_mov_b32_e32 v60, v182
	v_mov_b32_e32 v61, v183
	v_pk_fma_f32 v[48:49], v[48:49], v[50:51], v[60:61]
	v_pk_fma_f32 v[46:47], v[46:47], v[52:53], v[58:59]
	s_nop 0
	v_cvt_pk_bf16_f32 v46, v46, v47
	v_cvt_pk_bf16_f32 v47, v48, v49
	global_store_dwordx2 v[72:73], v[46:47], off offset:2048
	s_nop 0
	s_waitcnt vmcnt(21)
	v_mov_b32_e32 v46, v184
	v_mov_b32_e32 v47, v185
	v_mov_b32_e32 v48, v186
	v_mov_b32_e32 v49, v187
	v_pk_mul_f32 v[42:43], v[42:43], v[46:47]
	v_pk_mul_f32 v[44:45], v[44:45], v[48:49]
	s_waitcnt vmcnt(21)
	v_mov_b32_e32 v50, v188
	v_mov_b32_e32 v51, v189
	v_mov_b32_e32 v52, v190
	v_mov_b32_e32 v53, v191
	v_pk_add_f32 v[46:47], v[52:53], 1.0 op_sel_hi:[1,0]
	v_pk_add_f32 v[48:49], v[50:51], 1.0 op_sel_hi:[1,0]
	s_waitcnt vmcnt(21)
	v_mov_b32_e32 v54, v192
	v_mov_b32_e32 v55, v193
	v_mov_b32_e32 v56, v194
	v_mov_b32_e32 v57, v195
	v_pk_fma_f32 v[44:45], v[44:45], v[46:47], v[56:57]
	v_pk_fma_f32 v[42:43], v[42:43], v[48:49], v[54:55]
	s_nop 0
	v_cvt_pk_bf16_f32 v42, v42, v43
	v_cvt_pk_bf16_f32 v43, v44, v45
	global_store_dwordx2 v[72:73], v[42:43], off offset:2560
	s_nop 0
	s_waitcnt vmcnt(21)
	v_mov_b32_e32 v42, v196
	v_mov_b32_e32 v43, v197
	v_mov_b32_e32 v44, v198
	v_mov_b32_e32 v45, v199
	v_pk_mul_f32 v[38:39], v[38:39], v[42:43]
	v_pk_mul_f32 v[40:41], v[40:41], v[44:45]
	s_waitcnt vmcnt(21)
	v_mov_b32_e32 v46, v200
	v_mov_b32_e32 v47, v201
	v_mov_b32_e32 v48, v202
	v_mov_b32_e32 v49, v203
	v_pk_add_f32 v[42:43], v[48:49], 1.0 op_sel_hi:[1,0]
	v_pk_add_f32 v[44:45], v[46:47], 1.0 op_sel_hi:[1,0]
	s_waitcnt vmcnt(21)
	v_mov_b32_e32 v50, v204
	v_mov_b32_e32 v51, v205
	v_mov_b32_e32 v52, v206
	v_mov_b32_e32 v53, v207
	v_pk_fma_f32 v[40:41], v[40:41], v[42:43], v[52:53]
	v_pk_fma_f32 v[38:39], v[38:39], v[44:45], v[50:51]
	s_nop 0
	v_cvt_pk_bf16_f32 v38, v38, v39
	v_cvt_pk_bf16_f32 v39, v40, v41
	global_store_dwordx2 v[72:73], v[38:39], off offset:3072
	s_nop 0
	s_add_u32 s16, s10, 0x2000
	s_addc_u32 s17, s11, 0
	global_load_dwordx4 v[224:227], v66, s[16:17]
	global_load_dwordx4 v[236:239], v77, s[16:17]
	global_load_dwordx4 v[248:251], v78, s[16:17]
	global_load_dwordx4 v[116:119], v79, s[16:17]
	global_load_dwordx4 v[128:131], v80, s[16:17]
	global_load_dwordx4 v[140:143], v81, s[16:17]
	global_load_dwordx4 v[152:155], v82, s[16:17]
	global_load_dwordx4 v[164:167], v83, s[16:17]
	s_lshl_b64 s[2:3], s[14:15], 12
	s_waitcnt vmcnt(29)
	v_mov_b32_e32 v38, v208
	v_mov_b32_e32 v39, v209
	v_mov_b32_e32 v40, v210
	v_mov_b32_e32 v41, v211
	v_pk_mul_f32 v[26:27], v[26:27], v[38:39]
	v_pk_mul_f32 v[28:29], v[28:29], v[40:41]
	s_waitcnt vmcnt(29)
	v_mov_b32_e32 v42, v212
	v_mov_b32_e32 v43, v213
	v_mov_b32_e32 v44, v214
	v_mov_b32_e32 v45, v215
	v_pk_add_f32 v[38:39], v[44:45], 1.0 op_sel_hi:[1,0]
	v_pk_add_f32 v[40:41], v[42:43], 1.0 op_sel_hi:[1,0]
	s_waitcnt vmcnt(29)
	v_mov_b32_e32 v46, v216
	v_mov_b32_e32 v47, v217
	v_mov_b32_e32 v48, v218
	v_mov_b32_e32 v49, v219
	v_pk_fma_f32 v[28:29], v[28:29], v[38:39], v[48:49]
	v_pk_fma_f32 v[26:27], v[26:27], v[40:41], v[46:47]
	v_mul_f32_e32 v46, 0x4b800000, v96
	v_cvt_pk_bf16_f32 v26, v26, v27
	v_cvt_pk_bf16_f32 v27, v28, v29
	global_store_dwordx2 v[72:73], v[26:27], off offset:3584
	s_nop 0
	v_cndmask_b32_e32 v46, v96, v46, vcc
	v_rsq_f32_e32 v48, v46
	v_lshl_add_u64 v[46:47], v[70:71], 0, s[2:3]
	s_mov_b64 s[2:3], s[46:47]
	s_add_i32 s24, s24, s2
	v_mul_f32_e32 v49, 0x45800000, v48
	v_cndmask_b32_e32 v48, v48, v49, vcc
	v_pk_mul_f32 v[36:37], v[36:37], v[48:49] op_sel_hi:[1,0]
	v_pk_mul_f32 v[34:35], v[34:35], v[48:49] op_sel_hi:[1,0]
	v_pk_mul_f32 v[32:33], v[32:33], v[48:49] op_sel_hi:[1,0]
	v_pk_mul_f32 v[30:31], v[30:31], v[48:49] op_sel_hi:[1,0]
	v_pk_mul_f32 v[24:25], v[24:25], v[48:49] op_sel_hi:[1,0]
	v_pk_mul_f32 v[22:23], v[22:23], v[48:49] op_sel_hi:[1,0]
	v_pk_mul_f32 v[20:21], v[20:21], v[48:49] op_sel_hi:[1,0]
	v_pk_mul_f32 v[18:19], v[18:19], v[48:49] op_sel_hi:[1,0]
	v_pk_mul_f32 v[16:17], v[16:17], v[48:49] op_sel_hi:[1,0]
	v_pk_mul_f32 v[14:15], v[14:15], v[48:49] op_sel_hi:[1,0]
	v_pk_mul_f32 v[12:13], v[12:13], v[48:49] op_sel_hi:[1,0]
	v_pk_mul_f32 v[10:11], v[10:11], v[48:49] op_sel_hi:[1,0]
	v_pk_mul_f32 v[8:9], v[8:9], v[48:49] op_sel_hi:[1,0]
	v_pk_mul_f32 v[6:7], v[6:7], v[48:49] op_sel_hi:[1,0]
	v_pk_mul_f32 v[4:5], v[4:5], v[48:49] op_sel_hi:[1,0]
	v_pk_mul_f32 v[2:3], v[2:3], v[48:49] op_sel_hi:[1,0]
	s_add_u32 s6, s6, s2
	s_addc_u32 s7, s7, s3
	s_cmpk_gt_i32 s24, 0x43ff
	v_lshl_add_u64 v[72:73], v[72:73], 0, s[4:5]
	s_waitcnt vmcnt(29)
	v_mov_b32_e32 v26, v220
	v_mov_b32_e32 v27, v221
	v_mov_b32_e32 v28, v222
	v_mov_b32_e32 v29, v223
	v_pk_mul_f32 v[26:27], v[26:27], v[34:35]
	v_pk_mul_f32 v[28:29], v[28:29], v[36:37]
	s_waitcnt vmcnt(8)
	v_mov_b32_e32 v38, v224
	v_mov_b32_e32 v39, v225
	v_mov_b32_e32 v40, v226
	v_mov_b32_e32 v41, v227
	v_pk_add_f32 v[34:35], v[40:41], 1.0 op_sel_hi:[1,0]
	v_pk_add_f32 v[36:37], v[38:39], 1.0 op_sel_hi:[1,0]
	s_waitcnt vmcnt(8)
	v_mov_b32_e32 v42, v228
	v_mov_b32_e32 v43, v229
	v_mov_b32_e32 v44, v230
	v_mov_b32_e32 v45, v231
	v_pk_fma_f32 v[28:29], v[34:35], v[28:29], v[44:45]
	v_pk_fma_f32 v[26:27], v[36:37], v[26:27], v[42:43]
	s_nop 0
	v_cvt_pk_bf16_f32 v26, v26, v27
	v_cvt_pk_bf16_f32 v27, v28, v29
	global_store_dwordx2 v[46:47], v[26:27], off
	s_nop 0
	s_waitcnt vmcnt(9)
	v_mov_b32_e32 v26, v232
	v_mov_b32_e32 v27, v233
	v_mov_b32_e32 v28, v234
	v_mov_b32_e32 v29, v235
	v_pk_mul_f32 v[26:27], v[26:27], v[30:31]
	v_pk_mul_f32 v[28:29], v[28:29], v[32:33]
	s_waitcnt vmcnt(8)
	v_mov_b32_e32 v34, v236
	v_mov_b32_e32 v35, v237
	v_mov_b32_e32 v36, v238
	v_mov_b32_e32 v37, v239
	v_pk_add_f32 v[30:31], v[36:37], 1.0 op_sel_hi:[1,0]
	v_pk_add_f32 v[32:33], v[34:35], 1.0 op_sel_hi:[1,0]
	s_waitcnt vmcnt(8)
	v_mov_b32_e32 v38, v240
	v_mov_b32_e32 v39, v241
	v_mov_b32_e32 v40, v242
	v_mov_b32_e32 v41, v243
	v_pk_fma_f32 v[28:29], v[30:31], v[28:29], v[40:41]
	v_pk_fma_f32 v[26:27], v[32:33], v[26:27], v[38:39]
	s_nop 0
	v_cvt_pk_bf16_f32 v26, v26, v27
	v_cvt_pk_bf16_f32 v27, v28, v29
	global_store_dwordx2 v[46:47], v[26:27], off offset:512
	s_nop 0
	s_waitcnt vmcnt(9)
	v_mov_b32_e32 v26, v244
	v_mov_b32_e32 v27, v245
	v_mov_b32_e32 v28, v246
	v_mov_b32_e32 v29, v247
	v_pk_mul_f32 v[22:23], v[26:27], v[22:23]
	v_pk_mul_f32 v[24:25], v[28:29], v[24:25]
	s_waitcnt vmcnt(8)
	v_mov_b32_e32 v30, v248
	v_mov_b32_e32 v31, v249
	v_mov_b32_e32 v32, v250
	v_mov_b32_e32 v33, v251
	v_pk_add_f32 v[26:27], v[32:33], 1.0 op_sel_hi:[1,0]
	v_pk_add_f32 v[28:29], v[30:31], 1.0 op_sel_hi:[1,0]
	s_waitcnt vmcnt(8)
	v_mov_b32_e32 v34, v108
	v_mov_b32_e32 v35, v109
	v_mov_b32_e32 v36, v110
	v_mov_b32_e32 v37, v111
	v_pk_fma_f32 v[24:25], v[26:27], v[24:25], v[36:37]
	v_pk_fma_f32 v[22:23], v[28:29], v[22:23], v[34:35]
	s_nop 0
	v_cvt_pk_bf16_f32 v22, v22, v23
	v_cvt_pk_bf16_f32 v23, v24, v25
	global_store_dwordx2 v[46:47], v[22:23], off offset:1024
	s_nop 0
	s_waitcnt vmcnt(9)
	v_mov_b32_e32 v22, v112
	v_mov_b32_e32 v23, v113
	v_mov_b32_e32 v24, v114
	v_mov_b32_e32 v25, v115
	v_pk_mul_f32 v[18:19], v[22:23], v[18:19]
	v_pk_mul_f32 v[20:21], v[24:25], v[20:21]
	s_waitcnt vmcnt(8)
	v_mov_b32_e32 v26, v116
	v_mov_b32_e32 v27, v117
	v_mov_b32_e32 v28, v118
	v_mov_b32_e32 v29, v119
	v_pk_add_f32 v[22:23], v[28:29], 1.0 op_sel_hi:[1,0]
	v_pk_add_f32 v[24:25], v[26:27], 1.0 op_sel_hi:[1,0]
	s_waitcnt vmcnt(8)
	v_mov_b32_e32 v30, v120
	v_mov_b32_e32 v31, v121
	v_mov_b32_e32 v32, v122
	v_mov_b32_e32 v33, v123
	v_pk_fma_f32 v[20:21], v[20:21], v[22:23], v[32:33]
	v_pk_fma_f32 v[18:19], v[18:19], v[24:25], v[30:31]
	s_nop 0
	v_cvt_pk_bf16_f32 v18, v18, v19
	v_cvt_pk_bf16_f32 v19, v20, v21
	global_store_dwordx2 v[46:47], v[18:19], off offset:1536
	s_nop 0
	s_waitcnt vmcnt(9)
	v_mov_b32_e32 v18, v124
	v_mov_b32_e32 v19, v125
	v_mov_b32_e32 v20, v126
	v_mov_b32_e32 v21, v127
	v_pk_mul_f32 v[14:15], v[14:15], v[18:19]
	v_pk_mul_f32 v[16:17], v[16:17], v[20:21]
	s_waitcnt vmcnt(8)
	v_mov_b32_e32 v22, v128
	v_mov_b32_e32 v23, v129
	v_mov_b32_e32 v24, v130
	v_mov_b32_e32 v25, v131
	v_pk_add_f32 v[18:19], v[24:25], 1.0 op_sel_hi:[1,0]
	v_pk_add_f32 v[20:21], v[22:23], 1.0 op_sel_hi:[1,0]
	s_waitcnt vmcnt(8)
	v_mov_b32_e32 v26, v132
	v_mov_b32_e32 v27, v133
	v_mov_b32_e32 v28, v134
	v_mov_b32_e32 v29, v135
	v_pk_fma_f32 v[16:17], v[16:17], v[18:19], v[28:29]
	v_pk_fma_f32 v[14:15], v[14:15], v[20:21], v[26:27]
	s_nop 0
	v_cvt_pk_bf16_f32 v14, v14, v15
	v_cvt_pk_bf16_f32 v15, v16, v17
	global_store_dwordx2 v[46:47], v[14:15], off offset:2048
	s_nop 0
	s_waitcnt vmcnt(9)
	v_mov_b32_e32 v14, v136
	v_mov_b32_e32 v15, v137
	v_mov_b32_e32 v16, v138
	v_mov_b32_e32 v17, v139
	v_pk_mul_f32 v[10:11], v[10:11], v[14:15]
	v_pk_mul_f32 v[12:13], v[12:13], v[16:17]
	s_waitcnt vmcnt(8)
	v_mov_b32_e32 v18, v140
	v_mov_b32_e32 v19, v141
	v_mov_b32_e32 v20, v142
	v_mov_b32_e32 v21, v143
	v_pk_add_f32 v[14:15], v[20:21], 1.0 op_sel_hi:[1,0]
	v_pk_add_f32 v[16:17], v[18:19], 1.0 op_sel_hi:[1,0]
	s_waitcnt vmcnt(8)
	v_mov_b32_e32 v22, v144
	v_mov_b32_e32 v23, v145
	v_mov_b32_e32 v24, v146
	v_mov_b32_e32 v25, v147
	v_pk_fma_f32 v[12:13], v[12:13], v[14:15], v[24:25]
	v_pk_fma_f32 v[10:11], v[10:11], v[16:17], v[22:23]
	s_nop 0
	v_cvt_pk_bf16_f32 v10, v10, v11
	v_cvt_pk_bf16_f32 v11, v12, v13
	global_store_dwordx2 v[46:47], v[10:11], off offset:2560
	s_nop 0
	s_waitcnt vmcnt(9)
	v_mov_b32_e32 v10, v148
	v_mov_b32_e32 v11, v149
	v_mov_b32_e32 v12, v150
	v_mov_b32_e32 v13, v151
	v_pk_mul_f32 v[6:7], v[6:7], v[10:11]
	v_pk_mul_f32 v[8:9], v[8:9], v[12:13]
	s_waitcnt vmcnt(8)
	v_mov_b32_e32 v14, v152
	v_mov_b32_e32 v15, v153
	v_mov_b32_e32 v16, v154
	v_mov_b32_e32 v17, v155
	v_pk_add_f32 v[10:11], v[16:17], 1.0 op_sel_hi:[1,0]
	v_pk_add_f32 v[12:13], v[14:15], 1.0 op_sel_hi:[1,0]
	s_waitcnt vmcnt(8)
	v_mov_b32_e32 v18, v156
	v_mov_b32_e32 v19, v157
	v_mov_b32_e32 v20, v158
	v_mov_b32_e32 v21, v159
	v_pk_fma_f32 v[8:9], v[8:9], v[10:11], v[20:21]
	v_pk_fma_f32 v[6:7], v[6:7], v[12:13], v[18:19]
	s_nop 0
	v_cvt_pk_bf16_f32 v6, v6, v7
	v_cvt_pk_bf16_f32 v7, v8, v9
	global_store_dwordx2 v[46:47], v[6:7], off offset:3072
	s_nop 0
	s_waitcnt vmcnt(9)
	v_mov_b32_e32 v6, v160
	v_mov_b32_e32 v7, v161
	v_mov_b32_e32 v8, v162
	v_mov_b32_e32 v9, v163
	v_pk_mul_f32 v[2:3], v[2:3], v[6:7]
	v_pk_mul_f32 v[4:5], v[4:5], v[8:9]
	s_waitcnt vmcnt(8)
	v_mov_b32_e32 v10, v164
	v_mov_b32_e32 v11, v165
	v_mov_b32_e32 v12, v166
	v_mov_b32_e32 v13, v167
	v_pk_add_f32 v[6:7], v[12:13], 1.0 op_sel_hi:[1,0]
	v_pk_add_f32 v[8:9], v[10:11], 1.0 op_sel_hi:[1,0]
	s_waitcnt vmcnt(8)
	v_mov_b32_e32 v14, v168
	v_mov_b32_e32 v15, v169
	v_mov_b32_e32 v16, v170
	v_mov_b32_e32 v17, v171
	v_pk_fma_f32 v[4:5], v[4:5], v[6:7], v[16:17]
	v_pk_fma_f32 v[2:3], v[2:3], v[8:9], v[14:15]
	s_nop 0
	v_cvt_pk_bf16_f32 v2, v2, v3
	v_cvt_pk_bf16_f32 v3, v4, v5
	global_store_dwordx2 v[46:47], v[2:3], off offset:3584
	s_cbranch_scc1 .LBB0_396
